# waves 4-7 get s_setprio 1 in the first tile of each barrier block, nobody in the second
# speedup vs baseline: 1.0089x; 1.0058x over previous
.LBB0_734:
	s_cmp_eq_u32 s100, 0
	s_cbranch_scc1 .Lattn_pa0
	s_setprio 1
.Lattn_pa0:
	s_waitcnt lgkmcnt(6)
	v_mfma_f32_16x16x32_bf16 v[64:67], v[160:163], v[96:99], 0
	v_exp_f32_e32 v88, v88
	v_mfma_f32_16x16x32_bf16 v[68:71], v[160:163], v[112:115], 0
	v_exp_f32_e32 v92, v92
	ds_read_b128 v[234:237], v209 offset:6144
	s_add_u32 s16, s22, s10
	s_addc_u32 s17, s23, s11
	s_add_u32 s15, s22, s12
	s_addc_u32 s14, s23, s13
	s_add_u32 s8, s16, 0x3bc00200
	s_addc_u32 s9, s17, 0
	s_add_u32 s6, s15, 0x23a50000
	s_addc_u32 s7, s14, 0
	s_waitcnt lgkmcnt(6)
	v_mfma_f32_16x16x32_bf16 v[0:3], v[164:167], v[216:219], v[0:3]
	v_cvt_pk_bf16_f32 v242, v80, v81
	v_mfma_f32_16x16x32_bf16 v[4:7], v[164:167], v[238:241], v[4:7]
	v_exp_f32_e32 v89, v89
	ds_read_b128 v[160:163], v201 offset:20480
	s_waitcnt vmcnt(4)
	ds_write_b128 v225, v[152:155] offset:49152
	s_waitcnt lgkmcnt(7)
	v_mfma_f32_16x16x32_bf16 v[68:71], v[168:171], v[116:119], v[68:71]
	v_exp_f32_e32 v93, v93
	v_mfma_f32_16x16x32_bf16 v[64:67], v[168:171], v[100:103], v[64:67]
	v_cvt_pk_bf16_f32 v243, v82, v83
	ds_read_b128 v[164:167], v209 offset:8192
	ds_write_b128 v226, v[156:159] offset:49152
	s_waitcnt lgkmcnt(8)
	v_mfma_f32_16x16x32_bf16 v[12:15], v[172:175], v[238:241], v[12:15]
	v_exp_f32_e32 v90, v90
	v_mfma_f32_16x16x32_bf16 v[8:11], v[172:175], v[216:219], v[8:11]
	v_exp_f32_e32 v94, v94
	ds_read_b128 v[168:171], v202 offset:20480
	ds_write_b64 v227, v[132:133] offset:32768
	s_waitcnt lgkmcnt(9)
	v_mfma_f32_16x16x32_bf16 v[64:67], v[176:179], v[104:107], v[64:67]
	v_cvt_pk_bf16_f32 v204, v84, v85
	v_mfma_f32_16x16x32_bf16 v[68:71], v[176:179], v[120:123], v[68:71]
	v_exp_f32_e32 v91, v91
	ds_read_b128 v[172:175], v209 offset:10240
	ds_write_b64 v228, v[134:135] offset:32768
	s_waitcnt lgkmcnt(10)
	v_mfma_f32_16x16x32_bf16 v[16:19], v[180:183], v[216:219], v[16:19]
	v_exp_f32_e32 v95, v95
	v_mfma_f32_16x16x32_bf16 v[20:23], v[180:183], v[238:241], v[20:23]
	v_cvt_pk_bf16_f32 v205, v86, v87
	v_add_f32_e32 v220, v220, v88
	ds_read_b128 v[176:179], v203 offset:20480
	ds_write_b64 v229, v[128:129] offset:32768
	s_waitcnt lgkmcnt(11)
	v_mfma_f32_16x16x32_bf16 v[68:71], v[230:233], v[124:127], v[68:71]
	v_add_f32_e32 v221, v221, v92
	v_add_f32_e32 v220, v220, v89
	v_mfma_f32_16x16x32_bf16 v[64:67], v[230:233], v[108:111], v[64:67]
	v_add_f32_e32 v221, v221, v93
	v_cvt_pk_bf16_f32 v244, v88, v89
	ds_read_b128 v[180:183], v209 offset:12288
	ds_write_b64 v184, v[130:131] offset:32768
	s_waitcnt lgkmcnt(12)
	v_mfma_f32_16x16x32_bf16 v[28:31], v[234:237], v[238:241], v[28:31]
	v_cvt_pk_bf16_f32 v245, v90, v91
	v_cvt_pk_bf16_f32 v206, v92, v93
	v_mfma_f32_16x16x32_bf16 v[24:27], v[234:237], v[216:219], v[24:27]
	v_cvt_pk_bf16_f32 v207, v94, v95
	ds_read_b128 v[230:233], v246 offset:20480
	global_load_dwordx4 v[132:135], v198, s[8:9]
	s_waitcnt lgkmcnt(12)
	v_mfma_f32_16x16x32_bf16 v[72:75], v[160:163], v[96:99], 0
	v_add_f32_e32 v220, v220, v90
	v_add_f32_e32 v221, v221, v94
	v_mfma_f32_16x16x32_bf16 v[76:79], v[160:163], v[112:115], 0
	v_add_f32_e32 v220, v220, v91
	v_add_f32_e32 v221, v221, v95
	ds_read_b128 v[234:237], v209 offset:14336
	global_load_dwordx4 v[128:131], v199, s[8:9]
	s_waitcnt lgkmcnt(11)
	v_mfma_f32_16x16x32_bf16 v[32:35], v[164:167], v[216:219], v[32:35]
	v_add_f32_e32 v194, v194, v220
	v_add_f32_e32 v195, v195, v221
	v_mfma_f32_16x16x32_bf16 v[36:39], v[164:167], v[238:241], v[36:39]
	v_exp_f32_e32 v64, v64
	ds_read_b128 v[160:163], v201 offset:24576
	global_load_dwordx4 v[152:155], v196, s[6:7]
	s_waitcnt lgkmcnt(10)
	v_mfma_f32_16x16x32_bf16 v[76:79], v[168:171], v[116:119], v[76:79]
	v_exp_f32_e32 v68, v68
	v_mfma_f32_16x16x32_bf16 v[72:75], v[168:171], v[100:103], v[72:75]
	v_exp_f32_e32 v65, v65
	ds_read_b128 v[164:167], v210 offset:0
	global_load_dwordx4 v[156:159], v197, s[6:7]
	s_waitcnt lgkmcnt(9)
	v_mfma_f32_16x16x32_bf16 v[44:47], v[172:175], v[238:241], v[44:47]
	v_exp_f32_e32 v69, v69
	v_mfma_f32_16x16x32_bf16 v[40:43], v[172:175], v[216:219], v[40:43]
	v_exp_f32_e32 v66, v66
	ds_read_b128 v[168:171], v202 offset:24576
	s_waitcnt lgkmcnt(8)
	v_mfma_f32_16x16x32_bf16 v[72:75], v[176:179], v[104:107], v[72:75]
	v_exp_f32_e32 v70, v70
	v_mfma_f32_16x16x32_bf16 v[76:79], v[176:179], v[120:123], v[76:79]
	v_exp_f32_e32 v67, v67
	ds_read_b128 v[172:175], v210 offset:2048
	s_waitcnt lgkmcnt(7)
	v_mfma_f32_16x16x32_bf16 v[48:51], v[180:183], v[216:219], v[48:51]
	v_exp_f32_e32 v71, v71
	v_mfma_f32_16x16x32_bf16 v[52:55], v[180:183], v[238:241], v[52:55]
	v_add_f32_e32 v220, v64, v65
	ds_read_b128 v[176:179], v203 offset:24576
	s_waitcnt lgkmcnt(6)
	v_mfma_f32_16x16x32_bf16 v[76:79], v[230:233], v[124:127], v[76:79]
	v_add_f32_e32 v221, v68, v69
	v_mfma_f32_16x16x32_bf16 v[72:75], v[230:233], v[108:111], v[72:75]
	v_add_f32_e32 v220, v220, v66
	ds_read_b128 v[180:183], v210 offset:4096
	s_waitcnt lgkmcnt(6)
	v_mfma_f32_16x16x32_bf16 v[60:63], v[234:237], v[238:241], v[60:63]
	v_add_f32_e32 v221, v221, v70
	v_add_f32_e32 v220, v220, v67
	v_mfma_f32_16x16x32_bf16 v[56:59], v[234:237], v[216:219], v[56:59]
	v_add_f32_e32 v221, v221, v71
	ds_read_b128 v[230:233], v246 offset:24576
	s_waitcnt lgkmcnt(6)
	v_mfma_f32_16x16x32_bf16 v[80:83], v[160:163], v[96:99], 0
	v_exp_f32_e32 v72, v72
	v_mfma_f32_16x16x32_bf16 v[84:87], v[160:163], v[112:115], 0
	v_exp_f32_e32 v76, v76
	ds_read_b128 v[234:237], v210 offset:6144
	s_waitcnt lgkmcnt(6)
	v_mfma_f32_16x16x32_bf16 v[0:3], v[164:167], v[242:245], v[0:3]
	v_exp_f32_e32 v73, v73
	v_mfma_f32_16x16x32_bf16 v[4:7], v[164:167], v[204:207], v[4:7]
	v_exp_f32_e32 v77, v77
	ds_read_b128 v[160:163], v201 offset:28672
	s_waitcnt lgkmcnt(6)
	v_mfma_f32_16x16x32_bf16 v[84:87], v[168:171], v[116:119], v[84:87]
	v_exp_f32_e32 v74, v74
	v_mfma_f32_16x16x32_bf16 v[80:83], v[168:171], v[100:103], v[80:83]
	v_exp_f32_e32 v78, v78
	ds_read_b128 v[164:167], v210 offset:8192
	s_waitcnt lgkmcnt(6)
	v_mfma_f32_16x16x32_bf16 v[12:15], v[172:175], v[204:207], v[12:15]
	v_exp_f32_e32 v75, v75
	v_mfma_f32_16x16x32_bf16 v[8:11], v[172:175], v[242:245], v[8:11]
	v_exp_f32_e32 v79, v79
	ds_read_b128 v[168:171], v202 offset:28672
	s_waitcnt lgkmcnt(6)
	v_mfma_f32_16x16x32_bf16 v[80:83], v[176:179], v[104:107], v[80:83]
	v_add_f32_e32 v220, v220, v72
	v_add_f32_e32 v221, v221, v76
	v_mfma_f32_16x16x32_bf16 v[84:87], v[176:179], v[120:123], v[84:87]
	v_add_f32_e32 v220, v220, v73
	ds_read_b128 v[172:175], v210 offset:10240
	s_waitcnt lgkmcnt(6)
	v_mfma_f32_16x16x32_bf16 v[16:19], v[180:183], v[242:245], v[16:19]
	v_add_f32_e32 v221, v221, v77
	v_add_f32_e32 v220, v220, v74
	v_mfma_f32_16x16x32_bf16 v[20:23], v[180:183], v[204:207], v[20:23]
	v_add_f32_e32 v221, v221, v78
	ds_read_b128 v[176:179], v203 offset:28672
	s_waitcnt lgkmcnt(6)
	v_mfma_f32_16x16x32_bf16 v[84:87], v[230:233], v[124:127], v[84:87]
	v_add_f32_e32 v220, v220, v75
	v_add_f32_e32 v221, v221, v79
	v_mfma_f32_16x16x32_bf16 v[80:83], v[230:233], v[108:111], v[80:83]
	v_cvt_pk_bf16_f32 v216, v64, v65
	ds_read_b128 v[180:183], v210 offset:12288
	s_waitcnt lgkmcnt(6)
	v_mfma_f32_16x16x32_bf16 v[28:31], v[234:237], v[204:207], v[28:31]
	v_cvt_pk_bf16_f32 v217, v66, v67
	v_cvt_pk_bf16_f32 v238, v68, v69
	v_mfma_f32_16x16x32_bf16 v[24:27], v[234:237], v[242:245], v[24:27]
	v_cvt_pk_bf16_f32 v239, v70, v71
	ds_read_b128 v[230:233], v246 offset:28672
	s_waitcnt lgkmcnt(6)
	v_mfma_f32_16x16x32_bf16 v[88:91], v[160:163], v[96:99], 0
	v_exp_f32_e32 v80, v80
	v_mfma_f32_16x16x32_bf16 v[92:95], v[160:163], v[112:115], 0
	v_exp_f32_e32 v84, v84
	ds_read_b128 v[234:237], v210 offset:14336
	s_waitcnt lgkmcnt(6)
	v_mfma_f32_16x16x32_bf16 v[32:35], v[164:167], v[242:245], v[32:35]
	v_exp_f32_e32 v81, v81
	v_mfma_f32_16x16x32_bf16 v[36:39], v[164:167], v[204:207], v[36:39]
	v_exp_f32_e32 v85, v85
	ds_read_b128 v[160:163], v201 offset:32768
	s_waitcnt lgkmcnt(6)
	v_mfma_f32_16x16x32_bf16 v[92:95], v[168:171], v[116:119], v[92:95]
	v_exp_f32_e32 v82, v82
	v_mfma_f32_16x16x32_bf16 v[88:91], v[168:171], v[100:103], v[88:91]
	v_exp_f32_e32 v86, v86
	ds_read_b128 v[164:167], v209 offset:16384
	s_waitcnt lgkmcnt(6)
	v_mfma_f32_16x16x32_bf16 v[44:47], v[172:175], v[204:207], v[44:47]
	v_exp_f32_e32 v83, v83
	v_mfma_f32_16x16x32_bf16 v[40:43], v[172:175], v[242:245], v[40:43]
	v_exp_f32_e32 v87, v87
	ds_read_b128 v[168:171], v202 offset:32768
	s_waitcnt lgkmcnt(6)
	v_mfma_f32_16x16x32_bf16 v[88:91], v[176:179], v[104:107], v[88:91]
	v_add_f32_e32 v220, v220, v80
	v_add_f32_e32 v221, v221, v84
	v_mfma_f32_16x16x32_bf16 v[92:95], v[176:179], v[120:123], v[92:95]
	v_add_f32_e32 v220, v220, v81
	ds_read_b128 v[172:175], v209 offset:18432
	s_waitcnt lgkmcnt(6)
	v_mfma_f32_16x16x32_bf16 v[48:51], v[180:183], v[242:245], v[48:51]
	v_add_f32_e32 v221, v221, v85
	v_add_f32_e32 v220, v220, v82
	v_mfma_f32_16x16x32_bf16 v[52:55], v[180:183], v[204:207], v[52:55]
	v_add_f32_e32 v221, v221, v86
	ds_read_b128 v[176:179], v203 offset:32768
	s_waitcnt lgkmcnt(6)
	v_mfma_f32_16x16x32_bf16 v[92:95], v[230:233], v[124:127], v[92:95]
	v_add_f32_e32 v220, v220, v83
	v_add_f32_e32 v221, v221, v87
	v_mfma_f32_16x16x32_bf16 v[88:91], v[230:233], v[108:111], v[88:91]
	v_cvt_pk_bf16_f32 v218, v72, v73
	ds_read_b128 v[180:183], v209 offset:20480
	s_waitcnt lgkmcnt(6)
	v_mfma_f32_16x16x32_bf16 v[60:63], v[234:237], v[204:207], v[60:63]
	v_cvt_pk_bf16_f32 v219, v74, v75
	v_cvt_pk_bf16_f32 v240, v76, v77
	v_mfma_f32_16x16x32_bf16 v[56:59], v[234:237], v[242:245], v[56:59]
	v_cvt_pk_bf16_f32 v241, v78, v79
	ds_read_b128 v[230:233], v246 offset:32768
	s_setprio 0
	s_waitcnt lgkmcnt(6)
	v_mfma_f32_16x16x32_bf16 v[64:67], v[160:163], v[96:99], 0
	v_exp_f32_e32 v88, v88
	v_mfma_f32_16x16x32_bf16 v[68:71], v[160:163], v[112:115], 0
	v_exp_f32_e32 v92, v92
	ds_read_b128 v[234:237], v209 offset:22528
	s_add_u32 s8, s16, 0x3bc00280
	s_addc_u32 s9, s17, 0
	s_add_u32 s6, s15, 0x23a60000
	s_addc_u32 s7, s14, 0
	s_waitcnt lgkmcnt(6)
	v_mfma_f32_16x16x32_bf16 v[0:3], v[164:167], v[216:219], v[0:3]
	v_cvt_pk_bf16_f32 v242, v80, v81
	v_mfma_f32_16x16x32_bf16 v[4:7], v[164:167], v[238:241], v[4:7]
	v_exp_f32_e32 v89, v89
	ds_read_b128 v[160:163], v201 offset:36864
	s_waitcnt vmcnt(4)
	ds_write_b128 v225, v[136:139] offset:0
	s_waitcnt lgkmcnt(7)
	v_mfma_f32_16x16x32_bf16 v[68:71], v[168:171], v[116:119], v[68:71]
	v_exp_f32_e32 v93, v93
	v_mfma_f32_16x16x32_bf16 v[64:67], v[168:171], v[100:103], v[64:67]
	v_cvt_pk_bf16_f32 v243, v82, v83
	ds_read_b128 v[164:167], v209 offset:24576
	ds_write_b128 v226, v[140:143] offset:0
	s_waitcnt lgkmcnt(8)
	v_mfma_f32_16x16x32_bf16 v[12:15], v[172:175], v[238:241], v[12:15]
	v_exp_f32_e32 v90, v90
	v_mfma_f32_16x16x32_bf16 v[8:11], v[172:175], v[216:219], v[8:11]
	v_exp_f32_e32 v94, v94
	ds_read_b128 v[168:171], v202 offset:36864
	ds_write_b64 v227, v[148:149] offset:49152
	s_waitcnt lgkmcnt(9)
	v_mfma_f32_16x16x32_bf16 v[64:67], v[176:179], v[104:107], v[64:67]
	v_cvt_pk_bf16_f32 v204, v84, v85
	v_mfma_f32_16x16x32_bf16 v[68:71], v[176:179], v[120:123], v[68:71]
	v_exp_f32_e32 v91, v91
	ds_read_b128 v[172:175], v209 offset:26624
	ds_write_b64 v228, v[150:151] offset:49152
	s_waitcnt lgkmcnt(10)
	v_mfma_f32_16x16x32_bf16 v[16:19], v[180:183], v[216:219], v[16:19]
	v_exp_f32_e32 v95, v95
	v_mfma_f32_16x16x32_bf16 v[20:23], v[180:183], v[238:241], v[20:23]
	v_cvt_pk_bf16_f32 v205, v86, v87
	v_add_f32_e32 v220, v220, v88
	ds_read_b128 v[176:179], v203 offset:36864
	ds_write_b64 v229, v[144:145] offset:49152
	s_waitcnt lgkmcnt(11)
	v_mfma_f32_16x16x32_bf16 v[68:71], v[230:233], v[124:127], v[68:71]
	v_add_f32_e32 v221, v221, v92
	v_add_f32_e32 v220, v220, v89
	v_mfma_f32_16x16x32_bf16 v[64:67], v[230:233], v[108:111], v[64:67]
	v_add_f32_e32 v221, v221, v93
	v_cvt_pk_bf16_f32 v244, v88, v89
	ds_read_b128 v[180:183], v209 offset:28672
	ds_write_b64 v184, v[146:147] offset:49152
	s_waitcnt lgkmcnt(12)
	v_mfma_f32_16x16x32_bf16 v[28:31], v[234:237], v[238:241], v[28:31]
	v_cvt_pk_bf16_f32 v245, v90, v91
	v_cvt_pk_bf16_f32 v206, v92, v93
	v_mfma_f32_16x16x32_bf16 v[24:27], v[234:237], v[216:219], v[24:27]
	v_cvt_pk_bf16_f32 v207, v94, v95
	ds_read_b128 v[230:233], v246 offset:36864
	global_load_dwordx4 v[148:151], v198, s[8:9]
	s_waitcnt lgkmcnt(12)
	v_mfma_f32_16x16x32_bf16 v[72:75], v[160:163], v[96:99], 0
	v_add_f32_e32 v220, v220, v90
	v_add_f32_e32 v221, v221, v94
	v_mfma_f32_16x16x32_bf16 v[76:79], v[160:163], v[112:115], 0
	v_add_f32_e32 v220, v220, v91
	v_add_f32_e32 v221, v221, v95
	ds_read_b128 v[234:237], v209 offset:30720
	global_load_dwordx4 v[144:147], v199, s[8:9]
	s_waitcnt lgkmcnt(11)
	v_mfma_f32_16x16x32_bf16 v[32:35], v[164:167], v[216:219], v[32:35]
	v_add_f32_e32 v194, v194, v220
	v_add_f32_e32 v195, v195, v221
	v_mfma_f32_16x16x32_bf16 v[36:39], v[164:167], v[238:241], v[36:39]
	v_exp_f32_e32 v64, v64
	ds_read_b128 v[160:163], v201 offset:40960
	global_load_dwordx4 v[136:139], v196, s[6:7]
	s_waitcnt lgkmcnt(10)
	v_mfma_f32_16x16x32_bf16 v[76:79], v[168:171], v[116:119], v[76:79]
	v_exp_f32_e32 v68, v68
	v_mfma_f32_16x16x32_bf16 v[72:75], v[168:171], v[100:103], v[72:75]
	v_exp_f32_e32 v65, v65
	ds_read_b128 v[164:167], v210 offset:16384
	global_load_dwordx4 v[140:143], v197, s[6:7]
	s_waitcnt lgkmcnt(9)
	v_mfma_f32_16x16x32_bf16 v[44:47], v[172:175], v[238:241], v[44:47]
	v_exp_f32_e32 v69, v69
	v_mfma_f32_16x16x32_bf16 v[40:43], v[172:175], v[216:219], v[40:43]
	v_exp_f32_e32 v66, v66
	ds_read_b128 v[168:171], v202 offset:40960
	s_waitcnt lgkmcnt(8)
	v_mfma_f32_16x16x32_bf16 v[72:75], v[176:179], v[104:107], v[72:75]
	v_exp_f32_e32 v70, v70
	v_mfma_f32_16x16x32_bf16 v[76:79], v[176:179], v[120:123], v[76:79]
	v_exp_f32_e32 v67, v67
	ds_read_b128 v[172:175], v210 offset:18432
	s_waitcnt lgkmcnt(7)
	v_mfma_f32_16x16x32_bf16 v[48:51], v[180:183], v[216:219], v[48:51]
	v_exp_f32_e32 v71, v71
	v_mfma_f32_16x16x32_bf16 v[52:55], v[180:183], v[238:241], v[52:55]
	v_add_f32_e32 v220, v64, v65
	ds_read_b128 v[176:179], v203 offset:40960
	s_waitcnt lgkmcnt(6)
	v_mfma_f32_16x16x32_bf16 v[76:79], v[230:233], v[124:127], v[76:79]
	v_add_f32_e32 v221, v68, v69
	v_mfma_f32_16x16x32_bf16 v[72:75], v[230:233], v[108:111], v[72:75]
	v_add_f32_e32 v220, v220, v66
	ds_read_b128 v[180:183], v210 offset:20480
	s_waitcnt lgkmcnt(6)
	v_mfma_f32_16x16x32_bf16 v[60:63], v[234:237], v[238:241], v[60:63]
	v_add_f32_e32 v221, v221, v70
	v_add_f32_e32 v220, v220, v67
	v_mfma_f32_16x16x32_bf16 v[56:59], v[234:237], v[216:219], v[56:59]
	v_add_f32_e32 v221, v221, v71
	ds_read_b128 v[230:233], v246 offset:40960
	s_waitcnt lgkmcnt(6)
	v_mfma_f32_16x16x32_bf16 v[80:83], v[160:163], v[96:99], 0
	v_exp_f32_e32 v72, v72
	v_mfma_f32_16x16x32_bf16 v[84:87], v[160:163], v[112:115], 0
	v_exp_f32_e32 v76, v76
	ds_read_b128 v[234:237], v210 offset:22528
	s_waitcnt lgkmcnt(6)
	v_mfma_f32_16x16x32_bf16 v[0:3], v[164:167], v[242:245], v[0:3]
	v_exp_f32_e32 v73, v73
	v_mfma_f32_16x16x32_bf16 v[4:7], v[164:167], v[204:207], v[4:7]
	v_exp_f32_e32 v77, v77
	ds_read_b128 v[160:163], v201 offset:45056
	s_waitcnt lgkmcnt(6)
	v_mfma_f32_16x16x32_bf16 v[84:87], v[168:171], v[116:119], v[84:87]
	v_exp_f32_e32 v74, v74
	v_mfma_f32_16x16x32_bf16 v[80:83], v[168:171], v[100:103], v[80:83]
	v_exp_f32_e32 v78, v78
	ds_read_b128 v[164:167], v210 offset:24576
	s_waitcnt lgkmcnt(6)
	v_mfma_f32_16x16x32_bf16 v[12:15], v[172:175], v[204:207], v[12:15]
	v_exp_f32_e32 v75, v75
	v_mfma_f32_16x16x32_bf16 v[8:11], v[172:175], v[242:245], v[8:11]
	v_exp_f32_e32 v79, v79
	ds_read_b128 v[168:171], v202 offset:45056
	s_waitcnt lgkmcnt(6)
	v_mfma_f32_16x16x32_bf16 v[80:83], v[176:179], v[104:107], v[80:83]
	v_add_f32_e32 v220, v220, v72
	v_add_f32_e32 v221, v221, v76
	v_mfma_f32_16x16x32_bf16 v[84:87], v[176:179], v[120:123], v[84:87]
	v_add_f32_e32 v220, v220, v73
	ds_read_b128 v[172:175], v210 offset:26624
	s_waitcnt lgkmcnt(6)
	v_mfma_f32_16x16x32_bf16 v[16:19], v[180:183], v[242:245], v[16:19]
	v_add_f32_e32 v221, v221, v77
	v_add_f32_e32 v220, v220, v74
	v_mfma_f32_16x16x32_bf16 v[20:23], v[180:183], v[204:207], v[20:23]
	v_add_f32_e32 v221, v221, v78
	ds_read_b128 v[176:179], v203 offset:45056
	s_waitcnt lgkmcnt(6)
	v_mfma_f32_16x16x32_bf16 v[84:87], v[230:233], v[124:127], v[84:87]
	v_add_f32_e32 v220, v220, v75
	v_add_f32_e32 v221, v221, v79
	v_mfma_f32_16x16x32_bf16 v[80:83], v[230:233], v[108:111], v[80:83]
	v_cvt_pk_bf16_f32 v216, v64, v65
	ds_read_b128 v[180:183], v210 offset:28672
	s_waitcnt lgkmcnt(6)
	v_mfma_f32_16x16x32_bf16 v[28:31], v[234:237], v[204:207], v[28:31]
	v_cvt_pk_bf16_f32 v217, v66, v67
	v_cvt_pk_bf16_f32 v238, v68, v69
	v_mfma_f32_16x16x32_bf16 v[24:27], v[234:237], v[242:245], v[24:27]
	v_cvt_pk_bf16_f32 v239, v70, v71
	ds_read_b128 v[230:233], v246 offset:45056
	s_waitcnt lgkmcnt(6)
	v_mfma_f32_16x16x32_bf16 v[88:91], v[160:163], v[96:99], 0
	v_exp_f32_e32 v80, v80
	v_mfma_f32_16x16x32_bf16 v[92:95], v[160:163], v[112:115], 0
	v_exp_f32_e32 v84, v84
	ds_read_b128 v[234:237], v210 offset:30720
	s_waitcnt lgkmcnt(6)
	v_mfma_f32_16x16x32_bf16 v[32:35], v[164:167], v[242:245], v[32:35]
	v_exp_f32_e32 v81, v81
	v_mfma_f32_16x16x32_bf16 v[36:39], v[164:167], v[204:207], v[36:39]
	v_exp_f32_e32 v85, v85
	s_waitcnt lgkmcnt(5)
	v_mfma_f32_16x16x32_bf16 v[92:95], v[168:171], v[116:119], v[92:95]
	v_exp_f32_e32 v82, v82
	v_mfma_f32_16x16x32_bf16 v[88:91], v[168:171], v[100:103], v[88:91]
	v_exp_f32_e32 v86, v86
	s_waitcnt lgkmcnt(4)
	v_mfma_f32_16x16x32_bf16 v[44:47], v[172:175], v[204:207], v[44:47]
	v_exp_f32_e32 v83, v83
	v_mfma_f32_16x16x32_bf16 v[40:43], v[172:175], v[242:245], v[40:43]
	v_exp_f32_e32 v87, v87
	s_waitcnt lgkmcnt(3)
	v_mfma_f32_16x16x32_bf16 v[88:91], v[176:179], v[104:107], v[88:91]
	v_add_f32_e32 v220, v220, v80
	v_add_f32_e32 v221, v221, v84
	v_mfma_f32_16x16x32_bf16 v[92:95], v[176:179], v[120:123], v[92:95]
	v_add_f32_e32 v220, v220, v81
	s_waitcnt lgkmcnt(0)
	s_barrier
	ds_read_b128 v[160:163], v201 offset:49152
	ds_read_b128 v[164:167], v209 offset:32768
	ds_read_b128 v[168:171], v202 offset:49152
	ds_read_b128 v[172:175], v209 offset:34816
	v_mfma_f32_16x16x32_bf16 v[48:51], v[180:183], v[242:245], v[48:51]
	v_add_f32_e32 v221, v221, v85
	v_add_f32_e32 v220, v220, v82
	v_mfma_f32_16x16x32_bf16 v[52:55], v[180:183], v[204:207], v[52:55]
	v_add_f32_e32 v221, v221, v86
	ds_read_b128 v[176:179], v203 offset:49152
	v_mfma_f32_16x16x32_bf16 v[92:95], v[230:233], v[124:127], v[92:95]
	v_add_f32_e32 v220, v220, v83
	v_add_f32_e32 v221, v221, v87
	v_mfma_f32_16x16x32_bf16 v[88:91], v[230:233], v[108:111], v[88:91]
	v_cvt_pk_bf16_f32 v218, v72, v73
	ds_read_b128 v[180:183], v209 offset:36864
	v_mfma_f32_16x16x32_bf16 v[60:63], v[234:237], v[204:207], v[60:63]
	v_cvt_pk_bf16_f32 v219, v74, v75
	v_cvt_pk_bf16_f32 v240, v76, v77
	v_mfma_f32_16x16x32_bf16 v[56:59], v[234:237], v[242:245], v[56:59]
	v_cvt_pk_bf16_f32 v241, v78, v79
	ds_read_b128 v[230:233], v246 offset:49152
	s_cmp_eq_u32 s100, 0
	s_cbranch_scc1 .Lattn_pa2
	s_setprio 1
.Lattn_pa2:
	s_waitcnt lgkmcnt(6)
	v_mfma_f32_16x16x32_bf16 v[64:67], v[160:163], v[96:99], 0
	v_exp_f32_e32 v88, v88
	v_mfma_f32_16x16x32_bf16 v[68:71], v[160:163], v[112:115], 0
	v_exp_f32_e32 v92, v92
	ds_read_b128 v[234:237], v209 offset:38912
	s_add_u32 s8, s16, 0x3bc00300
	s_addc_u32 s9, s17, 0
	s_add_u32 s6, s15, 0x23a70000
	s_addc_u32 s7, s14, 0
	s_waitcnt lgkmcnt(6)
	v_mfma_f32_16x16x32_bf16 v[0:3], v[164:167], v[216:219], v[0:3]
	v_cvt_pk_bf16_f32 v242, v80, v81
	v_mfma_f32_16x16x32_bf16 v[4:7], v[164:167], v[238:241], v[4:7]
	v_exp_f32_e32 v89, v89
	ds_read_b128 v[160:163], v201 offset:53248
	s_waitcnt vmcnt(4)
	ds_write_b128 v225, v[152:155] offset:16384
	s_waitcnt lgkmcnt(7)
	v_mfma_f32_16x16x32_bf16 v[68:71], v[168:171], v[116:119], v[68:71]
	v_exp_f32_e32 v93, v93
	v_mfma_f32_16x16x32_bf16 v[64:67], v[168:171], v[100:103], v[64:67]
	v_cvt_pk_bf16_f32 v243, v82, v83
	ds_read_b128 v[164:167], v209 offset:40960
	ds_write_b128 v226, v[156:159] offset:16384
	s_waitcnt lgkmcnt(8)
	v_mfma_f32_16x16x32_bf16 v[12:15], v[172:175], v[238:241], v[12:15]
	v_exp_f32_e32 v90, v90
	v_mfma_f32_16x16x32_bf16 v[8:11], v[172:175], v[216:219], v[8:11]
	v_exp_f32_e32 v94, v94
	ds_read_b128 v[168:171], v202 offset:53248
	ds_write_b64 v227, v[132:133] offset:0
	s_waitcnt lgkmcnt(9)
	v_mfma_f32_16x16x32_bf16 v[64:67], v[176:179], v[104:107], v[64:67]
	v_cvt_pk_bf16_f32 v204, v84, v85
	v_mfma_f32_16x16x32_bf16 v[68:71], v[176:179], v[120:123], v[68:71]
	v_exp_f32_e32 v91, v91
	ds_read_b128 v[172:175], v209 offset:43008
	ds_write_b64 v228, v[134:135] offset:0
	s_waitcnt lgkmcnt(10)
	v_mfma_f32_16x16x32_bf16 v[16:19], v[180:183], v[216:219], v[16:19]
	v_exp_f32_e32 v95, v95
	v_mfma_f32_16x16x32_bf16 v[20:23], v[180:183], v[238:241], v[20:23]
	v_cvt_pk_bf16_f32 v205, v86, v87
	v_add_f32_e32 v220, v220, v88
	ds_read_b128 v[176:179], v203 offset:53248
	ds_write_b64 v229, v[128:129] offset:0
	s_waitcnt lgkmcnt(11)
	v_mfma_f32_16x16x32_bf16 v[68:71], v[230:233], v[124:127], v[68:71]
	v_add_f32_e32 v221, v221, v92
	v_add_f32_e32 v220, v220, v89
	v_mfma_f32_16x16x32_bf16 v[64:67], v[230:233], v[108:111], v[64:67]
	v_add_f32_e32 v221, v221, v93
	v_cvt_pk_bf16_f32 v244, v88, v89
	ds_read_b128 v[180:183], v209 offset:45056
	ds_write_b64 v184, v[130:131] offset:0
	s_waitcnt lgkmcnt(12)
	v_mfma_f32_16x16x32_bf16 v[28:31], v[234:237], v[238:241], v[28:31]
	v_cvt_pk_bf16_f32 v245, v90, v91
	v_cvt_pk_bf16_f32 v206, v92, v93
	v_mfma_f32_16x16x32_bf16 v[24:27], v[234:237], v[216:219], v[24:27]
	v_cvt_pk_bf16_f32 v207, v94, v95
	ds_read_b128 v[230:233], v246 offset:53248
	global_load_dwordx4 v[132:135], v198, s[8:9]
	s_waitcnt lgkmcnt(12)
	v_mfma_f32_16x16x32_bf16 v[72:75], v[160:163], v[96:99], 0
	v_add_f32_e32 v220, v220, v90
	v_add_f32_e32 v221, v221, v94
	v_mfma_f32_16x16x32_bf16 v[76:79], v[160:163], v[112:115], 0
	v_add_f32_e32 v220, v220, v91
	v_add_f32_e32 v221, v221, v95
	ds_read_b128 v[234:237], v209 offset:47104
	global_load_dwordx4 v[128:131], v199, s[8:9]
	s_waitcnt lgkmcnt(11)
	v_mfma_f32_16x16x32_bf16 v[32:35], v[164:167], v[216:219], v[32:35]
	v_add_f32_e32 v194, v194, v220
	v_add_f32_e32 v195, v195, v221
	v_mfma_f32_16x16x32_bf16 v[36:39], v[164:167], v[238:241], v[36:39]
	v_exp_f32_e32 v64, v64
	ds_read_b128 v[160:163], v201 offset:57344
	global_load_dwordx4 v[152:155], v196, s[6:7]
	s_waitcnt lgkmcnt(10)
	v_mfma_f32_16x16x32_bf16 v[76:79], v[168:171], v[116:119], v[76:79]
	v_exp_f32_e32 v68, v68
	v_mfma_f32_16x16x32_bf16 v[72:75], v[168:171], v[100:103], v[72:75]
	v_exp_f32_e32 v65, v65
	ds_read_b128 v[164:167], v210 offset:32768
	global_load_dwordx4 v[156:159], v197, s[6:7]
	s_waitcnt lgkmcnt(9)
	v_mfma_f32_16x16x32_bf16 v[44:47], v[172:175], v[238:241], v[44:47]
	v_exp_f32_e32 v69, v69
	v_mfma_f32_16x16x32_bf16 v[40:43], v[172:175], v[216:219], v[40:43]
	v_exp_f32_e32 v66, v66
	ds_read_b128 v[168:171], v202 offset:57344
	s_waitcnt lgkmcnt(8)
	v_mfma_f32_16x16x32_bf16 v[72:75], v[176:179], v[104:107], v[72:75]
	v_exp_f32_e32 v70, v70
	v_mfma_f32_16x16x32_bf16 v[76:79], v[176:179], v[120:123], v[76:79]
	v_exp_f32_e32 v67, v67
	ds_read_b128 v[172:175], v210 offset:34816
	s_waitcnt lgkmcnt(7)
	v_mfma_f32_16x16x32_bf16 v[48:51], v[180:183], v[216:219], v[48:51]
	v_exp_f32_e32 v71, v71
	v_mfma_f32_16x16x32_bf16 v[52:55], v[180:183], v[238:241], v[52:55]
	v_add_f32_e32 v220, v64, v65
	ds_read_b128 v[176:179], v203 offset:57344
	s_waitcnt lgkmcnt(6)
	v_mfma_f32_16x16x32_bf16 v[76:79], v[230:233], v[124:127], v[76:79]
	v_add_f32_e32 v221, v68, v69
	v_mfma_f32_16x16x32_bf16 v[72:75], v[230:233], v[108:111], v[72:75]
	v_add_f32_e32 v220, v220, v66
	ds_read_b128 v[180:183], v210 offset:36864
	s_waitcnt lgkmcnt(6)
	v_mfma_f32_16x16x32_bf16 v[60:63], v[234:237], v[238:241], v[60:63]
	v_add_f32_e32 v221, v221, v70
	v_add_f32_e32 v220, v220, v67
	v_mfma_f32_16x16x32_bf16 v[56:59], v[234:237], v[216:219], v[56:59]
	v_add_f32_e32 v221, v221, v71
	ds_read_b128 v[230:233], v246 offset:57344
	s_waitcnt lgkmcnt(6)
	v_mfma_f32_16x16x32_bf16 v[80:83], v[160:163], v[96:99], 0
	v_exp_f32_e32 v72, v72
	v_mfma_f32_16x16x32_bf16 v[84:87], v[160:163], v[112:115], 0
	v_exp_f32_e32 v76, v76
	ds_read_b128 v[234:237], v210 offset:38912
	s_waitcnt lgkmcnt(6)
	v_mfma_f32_16x16x32_bf16 v[0:3], v[164:167], v[242:245], v[0:3]
	v_exp_f32_e32 v73, v73
	v_mfma_f32_16x16x32_bf16 v[4:7], v[164:167], v[204:207], v[4:7]
	v_exp_f32_e32 v77, v77
	ds_read_b128 v[160:163], v201 offset:61440
	s_waitcnt lgkmcnt(6)
	v_mfma_f32_16x16x32_bf16 v[84:87], v[168:171], v[116:119], v[84:87]
	v_exp_f32_e32 v74, v74
	v_mfma_f32_16x16x32_bf16 v[80:83], v[168:171], v[100:103], v[80:83]
	v_exp_f32_e32 v78, v78
	ds_read_b128 v[164:167], v210 offset:40960
	s_waitcnt lgkmcnt(6)
	v_mfma_f32_16x16x32_bf16 v[12:15], v[172:175], v[204:207], v[12:15]
	v_exp_f32_e32 v75, v75
	v_mfma_f32_16x16x32_bf16 v[8:11], v[172:175], v[242:245], v[8:11]
	v_exp_f32_e32 v79, v79
	ds_read_b128 v[168:171], v202 offset:61440
	s_waitcnt lgkmcnt(6)
	v_mfma_f32_16x16x32_bf16 v[80:83], v[176:179], v[104:107], v[80:83]
	v_add_f32_e32 v220, v220, v72
	v_add_f32_e32 v221, v221, v76
	v_mfma_f32_16x16x32_bf16 v[84:87], v[176:179], v[120:123], v[84:87]
	v_add_f32_e32 v220, v220, v73
	ds_read_b128 v[172:175], v210 offset:43008
	s_waitcnt lgkmcnt(6)
	v_mfma_f32_16x16x32_bf16 v[16:19], v[180:183], v[242:245], v[16:19]
	v_add_f32_e32 v221, v221, v77
	v_add_f32_e32 v220, v220, v74
	v_mfma_f32_16x16x32_bf16 v[20:23], v[180:183], v[204:207], v[20:23]
	v_add_f32_e32 v221, v221, v78
	ds_read_b128 v[176:179], v203 offset:61440
	s_waitcnt lgkmcnt(6)
	v_mfma_f32_16x16x32_bf16 v[84:87], v[230:233], v[124:127], v[84:87]
	v_add_f32_e32 v220, v220, v75
	v_add_f32_e32 v221, v221, v79
	v_mfma_f32_16x16x32_bf16 v[80:83], v[230:233], v[108:111], v[80:83]
	v_cvt_pk_bf16_f32 v216, v64, v65
	ds_read_b128 v[180:183], v210 offset:45056
	s_waitcnt lgkmcnt(6)
	v_mfma_f32_16x16x32_bf16 v[28:31], v[234:237], v[204:207], v[28:31]
	v_cvt_pk_bf16_f32 v217, v66, v67
	v_cvt_pk_bf16_f32 v238, v68, v69
	v_mfma_f32_16x16x32_bf16 v[24:27], v[234:237], v[242:245], v[24:27]
	v_cvt_pk_bf16_f32 v239, v70, v71
	ds_read_b128 v[230:233], v246 offset:61440
	s_waitcnt lgkmcnt(6)
	v_mfma_f32_16x16x32_bf16 v[88:91], v[160:163], v[96:99], 0
	v_exp_f32_e32 v80, v80
	v_mfma_f32_16x16x32_bf16 v[92:95], v[160:163], v[112:115], 0
	v_exp_f32_e32 v84, v84
	ds_read_b128 v[234:237], v210 offset:47104
	s_waitcnt lgkmcnt(6)
	v_mfma_f32_16x16x32_bf16 v[32:35], v[164:167], v[242:245], v[32:35]
	v_exp_f32_e32 v81, v81
	v_mfma_f32_16x16x32_bf16 v[36:39], v[164:167], v[204:207], v[36:39]
	v_exp_f32_e32 v85, v85
	ds_read_b128 v[160:163], v201 offset:0
	s_waitcnt lgkmcnt(6)
	v_mfma_f32_16x16x32_bf16 v[92:95], v[168:171], v[116:119], v[92:95]
	v_exp_f32_e32 v82, v82
	v_mfma_f32_16x16x32_bf16 v[88:91], v[168:171], v[100:103], v[88:91]
	v_exp_f32_e32 v86, v86
	ds_read_b128 v[164:167], v209 offset:49152
	s_waitcnt lgkmcnt(6)
	v_mfma_f32_16x16x32_bf16 v[44:47], v[172:175], v[204:207], v[44:47]
	v_exp_f32_e32 v83, v83
	v_mfma_f32_16x16x32_bf16 v[40:43], v[172:175], v[242:245], v[40:43]
	v_exp_f32_e32 v87, v87
	ds_read_b128 v[168:171], v202 offset:0
	s_waitcnt lgkmcnt(6)
	v_mfma_f32_16x16x32_bf16 v[88:91], v[176:179], v[104:107], v[88:91]
	v_add_f32_e32 v220, v220, v80
	v_add_f32_e32 v221, v221, v84
	v_mfma_f32_16x16x32_bf16 v[92:95], v[176:179], v[120:123], v[92:95]
	v_add_f32_e32 v220, v220, v81
	ds_read_b128 v[172:175], v209 offset:51200
	s_waitcnt lgkmcnt(6)
	v_mfma_f32_16x16x32_bf16 v[48:51], v[180:183], v[242:245], v[48:51]
	v_add_f32_e32 v221, v221, v85
	v_add_f32_e32 v220, v220, v82
	v_mfma_f32_16x16x32_bf16 v[52:55], v[180:183], v[204:207], v[52:55]
	v_add_f32_e32 v221, v221, v86
	ds_read_b128 v[176:179], v203 offset:0
	s_waitcnt lgkmcnt(6)
	v_mfma_f32_16x16x32_bf16 v[92:95], v[230:233], v[124:127], v[92:95]
	v_add_f32_e32 v220, v220, v83
	v_add_f32_e32 v221, v221, v87
	v_mfma_f32_16x16x32_bf16 v[88:91], v[230:233], v[108:111], v[88:91]
	v_cvt_pk_bf16_f32 v218, v72, v73
	ds_read_b128 v[180:183], v209 offset:53248
	s_waitcnt lgkmcnt(6)
	v_mfma_f32_16x16x32_bf16 v[60:63], v[234:237], v[204:207], v[60:63]
	v_cvt_pk_bf16_f32 v219, v74, v75
	v_cvt_pk_bf16_f32 v240, v76, v77
	v_mfma_f32_16x16x32_bf16 v[56:59], v[234:237], v[242:245], v[56:59]
	v_cvt_pk_bf16_f32 v241, v78, v79
	ds_read_b128 v[230:233], v246 offset:0
	s_setprio 0
	s_waitcnt lgkmcnt(6)
	v_mfma_f32_16x16x32_bf16 v[64:67], v[160:163], v[96:99], 0
	v_exp_f32_e32 v88, v88
	v_mfma_f32_16x16x32_bf16 v[68:71], v[160:163], v[112:115], 0
	v_exp_f32_e32 v92, v92
	ds_read_b128 v[234:237], v209 offset:55296
	s_add_u32 s8, s16, 0x3bc00380
	s_addc_u32 s9, s17, 0
	s_add_u32 s6, s15, 0x23a80000
	s_addc_u32 s7, s14, 0
	s_waitcnt lgkmcnt(6)
	v_mfma_f32_16x16x32_bf16 v[0:3], v[164:167], v[216:219], v[0:3]
	v_cvt_pk_bf16_f32 v242, v80, v81
	v_mfma_f32_16x16x32_bf16 v[4:7], v[164:167], v[238:241], v[4:7]
	v_exp_f32_e32 v89, v89
	ds_read_b128 v[160:163], v201 offset:4096
	s_waitcnt vmcnt(4)
	ds_write_b128 v225, v[136:139] offset:32768
	s_waitcnt lgkmcnt(7)
	v_mfma_f32_16x16x32_bf16 v[68:71], v[168:171], v[116:119], v[68:71]
	v_exp_f32_e32 v93, v93
	v_mfma_f32_16x16x32_bf16 v[64:67], v[168:171], v[100:103], v[64:67]
	v_cvt_pk_bf16_f32 v243, v82, v83
	ds_read_b128 v[164:167], v209 offset:57344
	ds_write_b128 v226, v[140:143] offset:32768
	s_waitcnt lgkmcnt(8)
	v_mfma_f32_16x16x32_bf16 v[12:15], v[172:175], v[238:241], v[12:15]
	v_exp_f32_e32 v90, v90
	v_mfma_f32_16x16x32_bf16 v[8:11], v[172:175], v[216:219], v[8:11]
	v_exp_f32_e32 v94, v94
	ds_read_b128 v[168:171], v202 offset:4096
	ds_write_b64 v227, v[148:149] offset:16384
	s_waitcnt lgkmcnt(9)
	v_mfma_f32_16x16x32_bf16 v[64:67], v[176:179], v[104:107], v[64:67]
	v_cvt_pk_bf16_f32 v204, v84, v85
	v_mfma_f32_16x16x32_bf16 v[68:71], v[176:179], v[120:123], v[68:71]
	v_exp_f32_e32 v91, v91
	ds_read_b128 v[172:175], v209 offset:59392
	ds_write_b64 v228, v[150:151] offset:16384
	s_waitcnt lgkmcnt(10)
	v_mfma_f32_16x16x32_bf16 v[16:19], v[180:183], v[216:219], v[16:19]
	v_exp_f32_e32 v95, v95
	v_mfma_f32_16x16x32_bf16 v[20:23], v[180:183], v[238:241], v[20:23]
	v_cvt_pk_bf16_f32 v205, v86, v87
	v_add_f32_e32 v220, v220, v88
	ds_read_b128 v[176:179], v203 offset:4096
	ds_write_b64 v229, v[144:145] offset:16384
	s_waitcnt lgkmcnt(11)
	v_mfma_f32_16x16x32_bf16 v[68:71], v[230:233], v[124:127], v[68:71]
	v_add_f32_e32 v221, v221, v92
	v_add_f32_e32 v220, v220, v89
	v_mfma_f32_16x16x32_bf16 v[64:67], v[230:233], v[108:111], v[64:67]
	v_add_f32_e32 v221, v221, v93
	v_cvt_pk_bf16_f32 v244, v88, v89
	ds_read_b128 v[180:183], v209 offset:61440
	ds_write_b64 v184, v[146:147] offset:16384
	s_waitcnt lgkmcnt(12)
	v_mfma_f32_16x16x32_bf16 v[28:31], v[234:237], v[238:241], v[28:31]
	v_cvt_pk_bf16_f32 v245, v90, v91
	v_cvt_pk_bf16_f32 v206, v92, v93
	v_mfma_f32_16x16x32_bf16 v[24:27], v[234:237], v[216:219], v[24:27]
	v_cvt_pk_bf16_f32 v207, v94, v95
	ds_read_b128 v[230:233], v246 offset:4096
	global_load_dwordx4 v[148:151], v198, s[8:9]
	s_waitcnt lgkmcnt(12)
	v_mfma_f32_16x16x32_bf16 v[72:75], v[160:163], v[96:99], 0
	v_add_f32_e32 v220, v220, v90
	v_add_f32_e32 v221, v221, v94
	v_mfma_f32_16x16x32_bf16 v[76:79], v[160:163], v[112:115], 0
	v_add_f32_e32 v220, v220, v91
	v_add_f32_e32 v221, v221, v95
	ds_read_b128 v[234:237], v209 offset:63488
	global_load_dwordx4 v[144:147], v199, s[8:9]
	s_waitcnt lgkmcnt(11)
	v_mfma_f32_16x16x32_bf16 v[32:35], v[164:167], v[216:219], v[32:35]
	v_add_f32_e32 v194, v194, v220
	v_add_f32_e32 v195, v195, v221
	v_mfma_f32_16x16x32_bf16 v[36:39], v[164:167], v[238:241], v[36:39]
	v_exp_f32_e32 v64, v64
	ds_read_b128 v[160:163], v201 offset:8192
	global_load_dwordx4 v[136:139], v196, s[6:7]
	s_waitcnt lgkmcnt(10)
	v_mfma_f32_16x16x32_bf16 v[76:79], v[168:171], v[116:119], v[76:79]
	v_exp_f32_e32 v68, v68
	v_mfma_f32_16x16x32_bf16 v[72:75], v[168:171], v[100:103], v[72:75]
	v_exp_f32_e32 v65, v65
	ds_read_b128 v[164:167], v210 offset:49152
	global_load_dwordx4 v[140:143], v197, s[6:7]
	s_waitcnt lgkmcnt(9)
	v_mfma_f32_16x16x32_bf16 v[44:47], v[172:175], v[238:241], v[44:47]
	v_exp_f32_e32 v69, v69
	v_mfma_f32_16x16x32_bf16 v[40:43], v[172:175], v[216:219], v[40:43]
	v_exp_f32_e32 v66, v66
	ds_read_b128 v[168:171], v202 offset:8192
	s_waitcnt lgkmcnt(8)
	v_mfma_f32_16x16x32_bf16 v[72:75], v[176:179], v[104:107], v[72:75]
	v_exp_f32_e32 v70, v70
	v_mfma_f32_16x16x32_bf16 v[76:79], v[176:179], v[120:123], v[76:79]
	v_exp_f32_e32 v67, v67
	ds_read_b128 v[172:175], v210 offset:51200
	s_waitcnt lgkmcnt(7)
	v_mfma_f32_16x16x32_bf16 v[48:51], v[180:183], v[216:219], v[48:51]
	v_exp_f32_e32 v71, v71
	v_mfma_f32_16x16x32_bf16 v[52:55], v[180:183], v[238:241], v[52:55]
	v_add_f32_e32 v220, v64, v65
	ds_read_b128 v[176:179], v203 offset:8192
	s_waitcnt lgkmcnt(6)
	v_mfma_f32_16x16x32_bf16 v[76:79], v[230:233], v[124:127], v[76:79]
	v_add_f32_e32 v221, v68, v69
	v_mfma_f32_16x16x32_bf16 v[72:75], v[230:233], v[108:111], v[72:75]
	v_add_f32_e32 v220, v220, v66
	ds_read_b128 v[180:183], v210 offset:53248
	s_waitcnt lgkmcnt(6)
	v_mfma_f32_16x16x32_bf16 v[60:63], v[234:237], v[238:241], v[60:63]
	v_add_f32_e32 v221, v221, v70
	v_add_f32_e32 v220, v220, v67
	v_mfma_f32_16x16x32_bf16 v[56:59], v[234:237], v[216:219], v[56:59]
	v_add_f32_e32 v221, v221, v71
	ds_read_b128 v[230:233], v246 offset:8192
	s_waitcnt lgkmcnt(6)
	v_mfma_f32_16x16x32_bf16 v[80:83], v[160:163], v[96:99], 0
	v_exp_f32_e32 v72, v72
	v_mfma_f32_16x16x32_bf16 v[84:87], v[160:163], v[112:115], 0
	v_exp_f32_e32 v76, v76
	ds_read_b128 v[234:237], v210 offset:55296
	s_waitcnt lgkmcnt(6)
	v_mfma_f32_16x16x32_bf16 v[0:3], v[164:167], v[242:245], v[0:3]
	v_exp_f32_e32 v73, v73
	v_mfma_f32_16x16x32_bf16 v[4:7], v[164:167], v[204:207], v[4:7]
	v_exp_f32_e32 v77, v77
	ds_read_b128 v[160:163], v201 offset:12288
	s_waitcnt lgkmcnt(6)
	v_mfma_f32_16x16x32_bf16 v[84:87], v[168:171], v[116:119], v[84:87]
	v_exp_f32_e32 v74, v74
	v_mfma_f32_16x16x32_bf16 v[80:83], v[168:171], v[100:103], v[80:83]
	v_exp_f32_e32 v78, v78
	ds_read_b128 v[164:167], v210 offset:57344
	s_waitcnt lgkmcnt(6)
	v_mfma_f32_16x16x32_bf16 v[12:15], v[172:175], v[204:207], v[12:15]
	v_exp_f32_e32 v75, v75
	v_mfma_f32_16x16x32_bf16 v[8:11], v[172:175], v[242:245], v[8:11]
	v_exp_f32_e32 v79, v79
	ds_read_b128 v[168:171], v202 offset:12288
	s_waitcnt lgkmcnt(6)
	v_mfma_f32_16x16x32_bf16 v[80:83], v[176:179], v[104:107], v[80:83]
	v_add_f32_e32 v220, v220, v72
	v_add_f32_e32 v221, v221, v76
	v_mfma_f32_16x16x32_bf16 v[84:87], v[176:179], v[120:123], v[84:87]
	v_add_f32_e32 v220, v220, v73
	ds_read_b128 v[172:175], v210 offset:59392
	s_add_u32 s10, s10, 0x200
	s_addc_u32 s11, s11, 0
	s_add_u32 s12, s12, 0x40000
	s_addc_u32 s13, s13, 0
	s_add_i32 s4, s4, 4
	s_cmpk_lt_u32 s4, 0x104
	s_cselect_b64 s[6:7], -1, 0
	s_and_b64 s[6:7], s[0:1], s[6:7]
	s_and_b64 vcc, exec, s[6:7]
	s_waitcnt lgkmcnt(6)
	v_mfma_f32_16x16x32_bf16 v[16:19], v[180:183], v[242:245], v[16:19]
	v_add_f32_e32 v221, v221, v77
	v_add_f32_e32 v220, v220, v74
	v_mfma_f32_16x16x32_bf16 v[20:23], v[180:183], v[204:207], v[20:23]
	v_add_f32_e32 v221, v221, v78
	ds_read_b128 v[176:179], v203 offset:12288
	s_waitcnt lgkmcnt(6)
	v_mfma_f32_16x16x32_bf16 v[84:87], v[230:233], v[124:127], v[84:87]
	v_add_f32_e32 v220, v220, v75
	v_add_f32_e32 v221, v221, v79
	v_mfma_f32_16x16x32_bf16 v[80:83], v[230:233], v[108:111], v[80:83]
	v_cvt_pk_bf16_f32 v216, v64, v65
	ds_read_b128 v[180:183], v210 offset:61440
	s_waitcnt lgkmcnt(6)
	v_mfma_f32_16x16x32_bf16 v[28:31], v[234:237], v[204:207], v[28:31]
	v_cvt_pk_bf16_f32 v217, v66, v67
	v_cvt_pk_bf16_f32 v238, v68, v69
	v_mfma_f32_16x16x32_bf16 v[24:27], v[234:237], v[242:245], v[24:27]
	v_cvt_pk_bf16_f32 v239, v70, v71
	ds_read_b128 v[230:233], v246 offset:12288
	s_waitcnt lgkmcnt(6)
	v_mfma_f32_16x16x32_bf16 v[88:91], v[160:163], v[96:99], 0
	v_exp_f32_e32 v80, v80
	v_mfma_f32_16x16x32_bf16 v[92:95], v[160:163], v[112:115], 0
	v_exp_f32_e32 v84, v84
	ds_read_b128 v[234:237], v210 offset:63488
	s_waitcnt lgkmcnt(6)
	v_mfma_f32_16x16x32_bf16 v[32:35], v[164:167], v[242:245], v[32:35]
	v_exp_f32_e32 v81, v81
	v_mfma_f32_16x16x32_bf16 v[36:39], v[164:167], v[204:207], v[36:39]
	v_exp_f32_e32 v85, v85
	s_waitcnt lgkmcnt(5)
	v_mfma_f32_16x16x32_bf16 v[92:95], v[168:171], v[116:119], v[92:95]
	v_exp_f32_e32 v82, v82
	v_mfma_f32_16x16x32_bf16 v[88:91], v[168:171], v[100:103], v[88:91]
	v_exp_f32_e32 v86, v86
	s_waitcnt lgkmcnt(4)
	v_mfma_f32_16x16x32_bf16 v[44:47], v[172:175], v[204:207], v[44:47]
	v_exp_f32_e32 v83, v83
	v_mfma_f32_16x16x32_bf16 v[40:43], v[172:175], v[242:245], v[40:43]
	v_exp_f32_e32 v87, v87
	s_waitcnt lgkmcnt(3)
	v_mfma_f32_16x16x32_bf16 v[88:91], v[176:179], v[104:107], v[88:91]
	v_add_f32_e32 v220, v220, v80
	v_add_f32_e32 v221, v221, v84
	v_mfma_f32_16x16x32_bf16 v[92:95], v[176:179], v[120:123], v[92:95]
	v_add_f32_e32 v220, v220, v81
	s_waitcnt lgkmcnt(0)
	s_barrier
	ds_read_b128 v[160:163], v201 offset:16384
	ds_read_b128 v[164:167], v209 offset:0
	ds_read_b128 v[168:171], v202 offset:16384
	ds_read_b128 v[172:175], v209 offset:2048
	v_mfma_f32_16x16x32_bf16 v[48:51], v[180:183], v[242:245], v[48:51]
	v_add_f32_e32 v221, v221, v85
	v_add_f32_e32 v220, v220, v82
	v_mfma_f32_16x16x32_bf16 v[52:55], v[180:183], v[204:207], v[52:55]
	v_add_f32_e32 v221, v221, v86
	ds_read_b128 v[176:179], v203 offset:16384
	v_mfma_f32_16x16x32_bf16 v[92:95], v[230:233], v[124:127], v[92:95]
	v_add_f32_e32 v220, v220, v83
	v_add_f32_e32 v221, v221, v87
	v_mfma_f32_16x16x32_bf16 v[88:91], v[230:233], v[108:111], v[88:91]
	v_cvt_pk_bf16_f32 v218, v72, v73
	ds_read_b128 v[180:183], v209 offset:4096
	v_mfma_f32_16x16x32_bf16 v[60:63], v[234:237], v[204:207], v[60:63]
	v_cvt_pk_bf16_f32 v219, v74, v75
	v_cvt_pk_bf16_f32 v240, v76, v77
	v_mfma_f32_16x16x32_bf16 v[56:59], v[234:237], v[242:245], v[56:59]
	v_cvt_pk_bf16_f32 v241, v78, v79
	ds_read_b128 v[230:233], v246 offset:16384
	s_cbranch_vccnz .LBB0_734
	s_setprio 0
	s_waitcnt vmcnt(0)
	s_nop 7
	s_nop 7
	ds_swizzle_b32 v64, v194 offset:swizzle(SWAP,16)
	s_waitcnt lgkmcnt(0)
	v_add_f32_e32 v194, v194, v64
	v_mov_b32_e32 v65, v194
	s_nop 1
	v_permlane32_swap_b32_e32 v194, v65
	v_add_f32_e32 v194, v194, v65
	s_nop 0
	v_rcp_f32_e32 v66, v194
	ds_swizzle_b32 v64, v195 offset:swizzle(SWAP,16)
	s_waitcnt lgkmcnt(0)
	v_add_f32_e32 v195, v195, v64
	v_mov_b32_e32 v65, v195
	s_nop 1
	v_permlane32_swap_b32_e32 v195, v65
	v_add_f32_e32 v195, v195, v65
	s_nop 0
	v_rcp_f32_e32 v67, v195
	v_readlane_b32 s100, v250, 8
	v_mbcnt_lo_u32_b32 v68, -1, 0
	v_mbcnt_hi_u32_b32 v68, -1, v68
	v_and_b32_e32 v69, 15, v68
	v_lshrrev_b32_e32 v70, 4, v68
	s_lshr_b32 s101, s100, 1
	v_add_u32_e32 v69, s101, v69
	v_lshlrev_b32_e32 v69, 12, v69
	v_and_b32_e32 v71, 1, v70
	v_lshlrev_b32_e32 v71, 5, v71
	v_and_b32_e32 v70, 2, v70
	v_lshl_add_u32 v71, v70, 3, v71
	v_add_u32_e32 v70, v69, v71
	v_add_u32_e32 v71, 0x10000, v70
	v_mul_f32_e32 v0, v0, v66
	v_mul_f32_e32 v1, v1, v66
	v_mul_f32_e32 v2, v2, v66
	v_mul_f32_e32 v3, v3, v66
	v_mul_f32_e32 v8, v8, v66
	v_mul_f32_e32 v9, v9, v66
	v_mul_f32_e32 v10, v10, v66
	v_mul_f32_e32 v11, v11, v66
	v_cvt_pk_bf16_f32 v72, v0, v1
	v_cvt_pk_bf16_f32 v73, v2, v3
	v_cvt_pk_bf16_f32 v74, v8, v9
	v_cvt_pk_bf16_f32 v75, v10, v11
	s_nop 1
	v_permlane16_swap_b32_e32 v72, v74
	v_permlane16_swap_b32_e32 v73, v75
	s_nop 1
	global_store_dwordx4 v70, v[72:75], s[58:59] offset:0
	v_mul_f32_e32 v16, v16, v66
	v_mul_f32_e32 v17, v17, v66
	v_mul_f32_e32 v18, v18, v66
	v_mul_f32_e32 v19, v19, v66
	v_mul_f32_e32 v24, v24, v66
	v_mul_f32_e32 v25, v25, v66
	v_mul_f32_e32 v26, v26, v66
	v_mul_f32_e32 v27, v27, v66
	v_cvt_pk_bf16_f32 v76, v16, v17
	v_cvt_pk_bf16_f32 v77, v18, v19
	v_cvt_pk_bf16_f32 v78, v24, v25
	v_cvt_pk_bf16_f32 v79, v26, v27
	s_nop 1
	v_permlane16_swap_b32_e32 v76, v78
	v_permlane16_swap_b32_e32 v77, v79
	s_nop 1
	global_store_dwordx4 v70, v[76:79], s[58:59] offset:64
	v_mul_f32_e32 v32, v32, v66
	v_mul_f32_e32 v33, v33, v66
	v_mul_f32_e32 v34, v34, v66
	v_mul_f32_e32 v35, v35, v66
	v_mul_f32_e32 v40, v40, v66
	v_mul_f32_e32 v41, v41, v66
	v_mul_f32_e32 v42, v42, v66
	v_mul_f32_e32 v43, v43, v66
	v_cvt_pk_bf16_f32 v80, v32, v33
	v_cvt_pk_bf16_f32 v81, v34, v35
	v_cvt_pk_bf16_f32 v82, v40, v41
	v_cvt_pk_bf16_f32 v83, v42, v43
	s_nop 1
	v_permlane16_swap_b32_e32 v80, v82
	v_permlane16_swap_b32_e32 v81, v83
	s_nop 1
	global_store_dwordx4 v70, v[80:83], s[58:59] offset:128
	v_mul_f32_e32 v48, v48, v66
	v_mul_f32_e32 v49, v49, v66
	v_mul_f32_e32 v50, v50, v66
	v_mul_f32_e32 v51, v51, v66
	v_mul_f32_e32 v56, v56, v66
	v_mul_f32_e32 v57, v57, v66
	v_mul_f32_e32 v58, v58, v66
	v_mul_f32_e32 v59, v59, v66
	v_cvt_pk_bf16_f32 v84, v48, v49
	v_cvt_pk_bf16_f32 v85, v50, v51
	v_cvt_pk_bf16_f32 v86, v56, v57
	v_cvt_pk_bf16_f32 v87, v58, v59
	s_nop 1
	v_permlane16_swap_b32_e32 v84, v86
	v_permlane16_swap_b32_e32 v85, v87
	s_nop 1
	global_store_dwordx4 v70, v[84:87], s[58:59] offset:192
	v_mul_f32_e32 v4, v4, v67
	v_mul_f32_e32 v5, v5, v67
	v_mul_f32_e32 v6, v6, v67
	v_mul_f32_e32 v7, v7, v67
	v_mul_f32_e32 v12, v12, v67
	v_mul_f32_e32 v13, v13, v67
	v_mul_f32_e32 v14, v14, v67
	v_mul_f32_e32 v15, v15, v67
	v_cvt_pk_bf16_f32 v88, v4, v5
	v_cvt_pk_bf16_f32 v89, v6, v7
	v_cvt_pk_bf16_f32 v90, v12, v13
	v_cvt_pk_bf16_f32 v91, v14, v15
	s_nop 1
	v_permlane16_swap_b32_e32 v88, v90
	v_permlane16_swap_b32_e32 v89, v91
	s_nop 1
	global_store_dwordx4 v71, v[88:91], s[58:59] offset:0
	v_mul_f32_e32 v20, v20, v67
	v_mul_f32_e32 v21, v21, v67
	v_mul_f32_e32 v22, v22, v67
	v_mul_f32_e32 v23, v23, v67
	v_mul_f32_e32 v28, v28, v67
	v_mul_f32_e32 v29, v29, v67
	v_mul_f32_e32 v30, v30, v67
	v_mul_f32_e32 v31, v31, v67
	v_cvt_pk_bf16_f32 v92, v20, v21
	v_cvt_pk_bf16_f32 v93, v22, v23
	v_cvt_pk_bf16_f32 v94, v28, v29
	v_cvt_pk_bf16_f32 v95, v30, v31
	s_nop 1
	v_permlane16_swap_b32_e32 v92, v94
	v_permlane16_swap_b32_e32 v93, v95
	s_nop 1
	global_store_dwordx4 v71, v[92:95], s[58:59] offset:64
	v_mul_f32_e32 v36, v36, v67
	v_mul_f32_e32 v37, v37, v67
	v_mul_f32_e32 v38, v38, v67
	v_mul_f32_e32 v39, v39, v67
	v_mul_f32_e32 v44, v44, v67
	v_mul_f32_e32 v45, v45, v67
	v_mul_f32_e32 v46, v46, v67
	v_mul_f32_e32 v47, v47, v67
	v_cvt_pk_bf16_f32 v72, v36, v37
	v_cvt_pk_bf16_f32 v73, v38, v39
	v_cvt_pk_bf16_f32 v74, v44, v45
	v_cvt_pk_bf16_f32 v75, v46, v47
	s_nop 1
	v_permlane16_swap_b32_e32 v72, v74
	v_permlane16_swap_b32_e32 v73, v75
	s_nop 1
	global_store_dwordx4 v71, v[72:75], s[58:59] offset:128
	v_mul_f32_e32 v52, v52, v67
	v_mul_f32_e32 v53, v53, v67
	v_mul_f32_e32 v54, v54, v67
	v_mul_f32_e32 v55, v55, v67
	v_mul_f32_e32 v60, v60, v67
	v_mul_f32_e32 v61, v61, v67
	v_mul_f32_e32 v62, v62, v67
	v_mul_f32_e32 v63, v63, v67
	v_cvt_pk_bf16_f32 v76, v52, v53
	v_cvt_pk_bf16_f32 v77, v54, v55
	v_cvt_pk_bf16_f32 v78, v60, v61
	v_cvt_pk_bf16_f32 v79, v62, v63
	s_nop 1
	v_permlane16_swap_b32_e32 v76, v78
	v_permlane16_swap_b32_e32 v77, v79
	s_nop 1
	global_store_dwordx4 v71, v[76:79], s[58:59] offset:192
	s_barrier
